# attention loop: one s_waitcnt lgkmcnt per two LDS fragments instead of one per fragment
# baseline (speedup 1.0000x reference)
.Lattn_pb0:
	s_waitcnt lgkmcnt(5)
	v_mfma_f32_16x16x32_bf16 v[64:67], v[160:163], v[96:99], 0
	v_exp_f32_e32 v88, v88
	v_mfma_f32_16x16x32_bf16 v[68:71], v[160:163], v[112:115], 0
	v_exp_f32_e32 v92, v92
	ds_read_b128 v[234:237], v209 offset:6144
	s_add_u32 s16, s22, s10
	s_addc_u32 s17, s23, s11
	s_add_u32 s15, s22, s12
	s_addc_u32 s14, s23, s13
	s_add_u32 s8, s16, 0x3bc00200
	s_addc_u32 s9, s17, 0
	s_add_u32 s6, s15, 0x23a50000
	s_addc_u32 s7, s14, 0
	v_mfma_f32_16x16x32_bf16 v[0:3], v[164:167], v[216:219], v[0:3]
	v_cvt_pk_bf16_f32 v242, v80, v81
	v_mfma_f32_16x16x32_bf16 v[4:7], v[164:167], v[238:241], v[4:7]
	v_exp_f32_e32 v89, v89
	ds_read_b128 v[160:163], v201 offset:20480
	s_waitcnt vmcnt(4)
	ds_write_b128 v225, v[152:155] offset:49152
	s_waitcnt lgkmcnt(6)
	v_mfma_f32_16x16x32_bf16 v[68:71], v[168:171], v[116:119], v[68:71]
	v_exp_f32_e32 v93, v93
	v_mfma_f32_16x16x32_bf16 v[64:67], v[168:171], v[100:103], v[64:67]
	v_cvt_pk_bf16_f32 v243, v82, v83
	ds_read_b128 v[164:167], v209 offset:8192
	ds_write_b128 v226, v[156:159] offset:49152
	v_mfma_f32_16x16x32_bf16 v[12:15], v[172:175], v[238:241], v[12:15]
	v_exp_f32_e32 v90, v90
	v_mfma_f32_16x16x32_bf16 v[8:11], v[172:175], v[216:219], v[8:11]
	v_exp_f32_e32 v94, v94
	ds_read_b128 v[168:171], v202 offset:20480
	ds_write_b64 v227, v[132:133] offset:32768
	s_waitcnt lgkmcnt(8)
	v_mfma_f32_16x16x32_bf16 v[64:67], v[176:179], v[104:107], v[64:67]
	v_cvt_pk_bf16_f32 v204, v84, v85
	v_mfma_f32_16x16x32_bf16 v[68:71], v[176:179], v[120:123], v[68:71]
	v_exp_f32_e32 v91, v91
	ds_read_b128 v[172:175], v209 offset:10240
	ds_write_b64 v228, v[134:135] offset:32768
	v_mfma_f32_16x16x32_bf16 v[16:19], v[180:183], v[216:219], v[16:19]
	v_exp_f32_e32 v95, v95
	v_mfma_f32_16x16x32_bf16 v[20:23], v[180:183], v[238:241], v[20:23]
	v_cvt_pk_bf16_f32 v205, v86, v87
	v_add_f32_e32 v220, v220, v88
	ds_read_b128 v[176:179], v203 offset:20480
	ds_write_b64 v229, v[128:129] offset:32768
	s_waitcnt lgkmcnt(10)
	v_mfma_f32_16x16x32_bf16 v[68:71], v[230:233], v[124:127], v[68:71]
	v_add_f32_e32 v221, v221, v92
	v_add_f32_e32 v220, v220, v89
	v_mfma_f32_16x16x32_bf16 v[64:67], v[230:233], v[108:111], v[64:67]
	v_add_f32_e32 v221, v221, v93
	v_cvt_pk_bf16_f32 v244, v88, v89
	ds_read_b128 v[180:183], v209 offset:12288
	ds_write_b64 v184, v[130:131] offset:32768
	v_mfma_f32_16x16x32_bf16 v[28:31], v[234:237], v[238:241], v[28:31]
	v_cvt_pk_bf16_f32 v245, v90, v91
	v_cvt_pk_bf16_f32 v206, v92, v93
	v_mfma_f32_16x16x32_bf16 v[24:27], v[234:237], v[216:219], v[24:27]
	v_cvt_pk_bf16_f32 v207, v94, v95
	ds_read_b128 v[230:233], v246 offset:20480
	global_load_dwordx4 v[132:135], v198, s[8:9]
	s_waitcnt lgkmcnt(10)
	v_mfma_f32_16x16x32_bf16 v[72:75], v[160:163], v[96:99], 0
	v_add_f32_e32 v220, v220, v90
	v_add_f32_e32 v221, v221, v94
	v_mfma_f32_16x16x32_bf16 v[76:79], v[160:163], v[112:115], 0
	v_add_f32_e32 v220, v220, v91
	v_add_f32_e32 v221, v221, v95
	ds_read_b128 v[234:237], v209 offset:14336
	global_load_dwordx4 v[128:131], v199, s[8:9]
	v_mfma_f32_16x16x32_bf16 v[32:35], v[164:167], v[216:219], v[32:35]
	v_add_f32_e32 v194, v194, v220
	v_add_f32_e32 v195, v195, v221
	v_mfma_f32_16x16x32_bf16 v[36:39], v[164:167], v[238:241], v[36:39]
	v_exp_f32_e32 v64, v64
	ds_read_b128 v[160:163], v201 offset:24576
	global_load_dwordx4 v[152:155], v196, s[6:7]
	s_waitcnt lgkmcnt(8)
	v_mfma_f32_16x16x32_bf16 v[76:79], v[168:171], v[116:119], v[76:79]
	v_exp_f32_e32 v68, v68
	v_mfma_f32_16x16x32_bf16 v[72:75], v[168:171], v[100:103], v[72:75]
	v_exp_f32_e32 v65, v65
	ds_read_b128 v[164:167], v210 offset:0
	global_load_dwordx4 v[156:159], v197, s[6:7]
	v_mfma_f32_16x16x32_bf16 v[44:47], v[172:175], v[238:241], v[44:47]
	v_exp_f32_e32 v69, v69
	v_mfma_f32_16x16x32_bf16 v[40:43], v[172:175], v[216:219], v[40:43]
	v_exp_f32_e32 v66, v66
	ds_read_b128 v[168:171], v202 offset:24576
	s_waitcnt lgkmcnt(6)
	v_mfma_f32_16x16x32_bf16 v[72:75], v[176:179], v[104:107], v[72:75]
	v_exp_f32_e32 v70, v70
	v_mfma_f32_16x16x32_bf16 v[76:79], v[176:179], v[120:123], v[76:79]
	v_exp_f32_e32 v67, v67
	ds_read_b128 v[172:175], v210 offset:2048
	v_mfma_f32_16x16x32_bf16 v[48:51], v[180:183], v[216:219], v[48:51]
	v_exp_f32_e32 v71, v71
	v_mfma_f32_16x16x32_bf16 v[52:55], v[180:183], v[238:241], v[52:55]
	v_add_f32_e32 v220, v64, v65
	ds_read_b128 v[176:179], v203 offset:24576
	s_waitcnt lgkmcnt(5)
	v_mfma_f32_16x16x32_bf16 v[76:79], v[230:233], v[124:127], v[76:79]
	v_add_f32_e32 v221, v68, v69
	v_mfma_f32_16x16x32_bf16 v[72:75], v[230:233], v[108:111], v[72:75]
	v_add_f32_e32 v220, v220, v66
	ds_read_b128 v[180:183], v210 offset:4096
	v_mfma_f32_16x16x32_bf16 v[60:63], v[234:237], v[238:241], v[60:63]
	v_add_f32_e32 v221, v221, v70
	v_add_f32_e32 v220, v220, v67
	v_mfma_f32_16x16x32_bf16 v[56:59], v[234:237], v[216:219], v[56:59]
	v_add_f32_e32 v221, v221, v71
	ds_read_b128 v[230:233], v246 offset:24576
	s_waitcnt lgkmcnt(5)
	v_mfma_f32_16x16x32_bf16 v[80:83], v[160:163], v[96:99], 0
	v_exp_f32_e32 v72, v72
	v_mfma_f32_16x16x32_bf16 v[84:87], v[160:163], v[112:115], 0
	v_exp_f32_e32 v76, v76
	ds_read_b128 v[234:237], v210 offset:6144
	v_mfma_f32_16x16x32_bf16 v[0:3], v[164:167], v[242:245], v[0:3]
	v_exp_f32_e32 v73, v73
	v_mfma_f32_16x16x32_bf16 v[4:7], v[164:167], v[204:207], v[4:7]
	v_exp_f32_e32 v77, v77
	ds_read_b128 v[160:163], v201 offset:28672
	s_waitcnt lgkmcnt(5)
	v_mfma_f32_16x16x32_bf16 v[84:87], v[168:171], v[116:119], v[84:87]
	v_exp_f32_e32 v74, v74
	v_mfma_f32_16x16x32_bf16 v[80:83], v[168:171], v[100:103], v[80:83]
	v_exp_f32_e32 v78, v78
	ds_read_b128 v[164:167], v210 offset:8192
	v_mfma_f32_16x16x32_bf16 v[12:15], v[172:175], v[204:207], v[12:15]
	v_exp_f32_e32 v75, v75
	v_mfma_f32_16x16x32_bf16 v[8:11], v[172:175], v[242:245], v[8:11]
	v_exp_f32_e32 v79, v79
	ds_read_b128 v[168:171], v202 offset:28672
	s_waitcnt lgkmcnt(5)
	v_mfma_f32_16x16x32_bf16 v[80:83], v[176:179], v[104:107], v[80:83]
	v_add_f32_e32 v220, v220, v72
	v_add_f32_e32 v221, v221, v76
	v_mfma_f32_16x16x32_bf16 v[84:87], v[176:179], v[120:123], v[84:87]
	v_add_f32_e32 v220, v220, v73
	ds_read_b128 v[172:175], v210 offset:10240
	v_mfma_f32_16x16x32_bf16 v[16:19], v[180:183], v[242:245], v[16:19]
	v_add_f32_e32 v221, v221, v77
	v_add_f32_e32 v220, v220, v74
	v_mfma_f32_16x16x32_bf16 v[20:23], v[180:183], v[204:207], v[20:23]
	v_add_f32_e32 v221, v221, v78
	ds_read_b128 v[176:179], v203 offset:28672
	s_waitcnt lgkmcnt(5)
	v_mfma_f32_16x16x32_bf16 v[84:87], v[230:233], v[124:127], v[84:87]
	v_add_f32_e32 v220, v220, v75
	v_add_f32_e32 v221, v221, v79
	v_mfma_f32_16x16x32_bf16 v[80:83], v[230:233], v[108:111], v[80:83]
	v_cvt_pk_bf16_f32 v216, v64, v65
	ds_read_b128 v[180:183], v210 offset:12288
	v_mfma_f32_16x16x32_bf16 v[28:31], v[234:237], v[204:207], v[28:31]
	v_cvt_pk_bf16_f32 v217, v66, v67
	v_cvt_pk_bf16_f32 v238, v68, v69
	v_mfma_f32_16x16x32_bf16 v[24:27], v[234:237], v[242:245], v[24:27]
	v_cvt_pk_bf16_f32 v239, v70, v71
	ds_read_b128 v[230:233], v246 offset:28672
	s_waitcnt lgkmcnt(5)
	v_mfma_f32_16x16x32_bf16 v[88:91], v[160:163], v[96:99], 0
	v_exp_f32_e32 v80, v80
	v_mfma_f32_16x16x32_bf16 v[92:95], v[160:163], v[112:115], 0
	v_exp_f32_e32 v84, v84
	ds_read_b128 v[234:237], v210 offset:14336
	v_mfma_f32_16x16x32_bf16 v[32:35], v[164:167], v[242:245], v[32:35]
	v_exp_f32_e32 v81, v81
	v_mfma_f32_16x16x32_bf16 v[36:39], v[164:167], v[204:207], v[36:39]
	v_exp_f32_e32 v85, v85
	ds_read_b128 v[160:163], v201 offset:32768
	s_waitcnt lgkmcnt(5)
	v_mfma_f32_16x16x32_bf16 v[92:95], v[168:171], v[116:119], v[92:95]
	v_exp_f32_e32 v82, v82
	v_mfma_f32_16x16x32_bf16 v[88:91], v[168:171], v[100:103], v[88:91]
	v_exp_f32_e32 v86, v86
	ds_read_b128 v[164:167], v209 offset:16384
	v_mfma_f32_16x16x32_bf16 v[44:47], v[172:175], v[204:207], v[44:47]
	v_exp_f32_e32 v83, v83
	v_mfma_f32_16x16x32_bf16 v[40:43], v[172:175], v[242:245], v[40:43]
	v_exp_f32_e32 v87, v87
	ds_read_b128 v[168:171], v202 offset:32768
	s_waitcnt lgkmcnt(5)
	v_mfma_f32_16x16x32_bf16 v[88:91], v[176:179], v[104:107], v[88:91]
	v_add_f32_e32 v220, v220, v80
	v_add_f32_e32 v221, v221, v84
	v_mfma_f32_16x16x32_bf16 v[92:95], v[176:179], v[120:123], v[92:95]
	v_add_f32_e32 v220, v220, v81
	ds_read_b128 v[172:175], v209 offset:18432
	v_mfma_f32_16x16x32_bf16 v[48:51], v[180:183], v[242:245], v[48:51]
	v_add_f32_e32 v221, v221, v85
	v_add_f32_e32 v220, v220, v82
	v_mfma_f32_16x16x32_bf16 v[52:55], v[180:183], v[204:207], v[52:55]
	v_add_f32_e32 v221, v221, v86
	ds_read_b128 v[176:179], v203 offset:32768
	s_waitcnt lgkmcnt(5)
	v_mfma_f32_16x16x32_bf16 v[92:95], v[230:233], v[124:127], v[92:95]
	v_add_f32_e32 v220, v220, v83
	v_add_f32_e32 v221, v221, v87
	v_mfma_f32_16x16x32_bf16 v[88:91], v[230:233], v[108:111], v[88:91]
	v_cvt_pk_bf16_f32 v218, v72, v73
	ds_read_b128 v[180:183], v209 offset:20480
	v_mfma_f32_16x16x32_bf16 v[60:63], v[234:237], v[204:207], v[60:63]
	v_cvt_pk_bf16_f32 v219, v74, v75
	v_cvt_pk_bf16_f32 v240, v76, v77
	v_mfma_f32_16x16x32_bf16 v[56:59], v[234:237], v[242:245], v[56:59]
	v_cvt_pk_bf16_f32 v241, v78, v79
	ds_read_b128 v[230:233], v246 offset:32768
	s_cmp_eq_u32 s100, 1
	s_cbranch_scc1 .Lattn_pa1
	s_setprio 1
	s_branch .Lattn_pb1

.Lattn_pb1:
	s_waitcnt lgkmcnt(5)
	v_mfma_f32_16x16x32_bf16 v[64:67], v[160:163], v[96:99], 0
	v_exp_f32_e32 v88, v88
	v_mfma_f32_16x16x32_bf16 v[68:71], v[160:163], v[112:115], 0
	v_exp_f32_e32 v92, v92
	ds_read_b128 v[234:237], v209 offset:22528
	s_add_u32 s8, s16, 0x3bc00280
	s_addc_u32 s9, s17, 0
	s_add_u32 s6, s15, 0x23a60000
	s_addc_u32 s7, s14, 0
	v_mfma_f32_16x16x32_bf16 v[0:3], v[164:167], v[216:219], v[0:3]
	v_cvt_pk_bf16_f32 v242, v80, v81
	v_mfma_f32_16x16x32_bf16 v[4:7], v[164:167], v[238:241], v[4:7]
	v_exp_f32_e32 v89, v89
	ds_read_b128 v[160:163], v201 offset:36864
	s_waitcnt vmcnt(4)
	ds_write_b128 v225, v[136:139] offset:0
	s_waitcnt lgkmcnt(6)
	v_mfma_f32_16x16x32_bf16 v[68:71], v[168:171], v[116:119], v[68:71]
	v_exp_f32_e32 v93, v93
	v_mfma_f32_16x16x32_bf16 v[64:67], v[168:171], v[100:103], v[64:67]
	v_cvt_pk_bf16_f32 v243, v82, v83
	ds_read_b128 v[164:167], v209 offset:24576
	ds_write_b128 v226, v[140:143] offset:0
	v_mfma_f32_16x16x32_bf16 v[12:15], v[172:175], v[238:241], v[12:15]
	v_exp_f32_e32 v90, v90
	v_mfma_f32_16x16x32_bf16 v[8:11], v[172:175], v[216:219], v[8:11]
	v_exp_f32_e32 v94, v94
	ds_read_b128 v[168:171], v202 offset:36864
	ds_write_b64 v227, v[148:149] offset:49152
	s_waitcnt lgkmcnt(8)
	v_mfma_f32_16x16x32_bf16 v[64:67], v[176:179], v[104:107], v[64:67]
	v_cvt_pk_bf16_f32 v204, v84, v85
	v_mfma_f32_16x16x32_bf16 v[68:71], v[176:179], v[120:123], v[68:71]
	v_exp_f32_e32 v91, v91
	ds_read_b128 v[172:175], v209 offset:26624
	ds_write_b64 v228, v[150:151] offset:49152
	v_mfma_f32_16x16x32_bf16 v[16:19], v[180:183], v[216:219], v[16:19]
	v_exp_f32_e32 v95, v95
	v_mfma_f32_16x16x32_bf16 v[20:23], v[180:183], v[238:241], v[20:23]
	v_cvt_pk_bf16_f32 v205, v86, v87
	v_add_f32_e32 v220, v220, v88
	ds_read_b128 v[176:179], v203 offset:36864
	ds_write_b64 v229, v[144:145] offset:49152
	s_waitcnt lgkmcnt(10)
	v_mfma_f32_16x16x32_bf16 v[68:71], v[230:233], v[124:127], v[68:71]
	v_add_f32_e32 v221, v221, v92
	v_add_f32_e32 v220, v220, v89
	v_mfma_f32_16x16x32_bf16 v[64:67], v[230:233], v[108:111], v[64:67]
	v_add_f32_e32 v221, v221, v93
	v_cvt_pk_bf16_f32 v244, v88, v89
	ds_read_b128 v[180:183], v209 offset:28672
	ds_write_b64 v184, v[146:147] offset:49152
	v_mfma_f32_16x16x32_bf16 v[28:31], v[234:237], v[238:241], v[28:31]
	v_cvt_pk_bf16_f32 v245, v90, v91
	v_cvt_pk_bf16_f32 v206, v92, v93
	v_mfma_f32_16x16x32_bf16 v[24:27], v[234:237], v[216:219], v[24:27]
	v_cvt_pk_bf16_f32 v207, v94, v95
	ds_read_b128 v[230:233], v246 offset:36864
	global_load_dwordx4 v[148:151], v198, s[8:9]
	s_waitcnt lgkmcnt(10)
	v_mfma_f32_16x16x32_bf16 v[72:75], v[160:163], v[96:99], 0
	v_add_f32_e32 v220, v220, v90
	v_add_f32_e32 v221, v221, v94
	v_mfma_f32_16x16x32_bf16 v[76:79], v[160:163], v[112:115], 0
	v_add_f32_e32 v220, v220, v91
	v_add_f32_e32 v221, v221, v95
	ds_read_b128 v[234:237], v209 offset:30720
	global_load_dwordx4 v[144:147], v199, s[8:9]
	v_mfma_f32_16x16x32_bf16 v[32:35], v[164:167], v[216:219], v[32:35]
	v_add_f32_e32 v194, v194, v220
	v_add_f32_e32 v195, v195, v221
	v_mfma_f32_16x16x32_bf16 v[36:39], v[164:167], v[238:241], v[36:39]
	v_exp_f32_e32 v64, v64
	ds_read_b128 v[160:163], v201 offset:40960
	global_load_dwordx4 v[136:139], v196, s[6:7]
	s_waitcnt lgkmcnt(8)
	v_mfma_f32_16x16x32_bf16 v[76:79], v[168:171], v[116:119], v[76:79]
	v_exp_f32_e32 v68, v68
	v_mfma_f32_16x16x32_bf16 v[72:75], v[168:171], v[100:103], v[72:75]
	v_exp_f32_e32 v65, v65
	ds_read_b128 v[164:167], v210 offset:16384
	global_load_dwordx4 v[140:143], v197, s[6:7]
	v_mfma_f32_16x16x32_bf16 v[44:47], v[172:175], v[238:241], v[44:47]
	v_exp_f32_e32 v69, v69
	v_mfma_f32_16x16x32_bf16 v[40:43], v[172:175], v[216:219], v[40:43]
	v_exp_f32_e32 v66, v66
	ds_read_b128 v[168:171], v202 offset:40960
	s_waitcnt lgkmcnt(6)
	v_mfma_f32_16x16x32_bf16 v[72:75], v[176:179], v[104:107], v[72:75]
	v_exp_f32_e32 v70, v70
	v_mfma_f32_16x16x32_bf16 v[76:79], v[176:179], v[120:123], v[76:79]
	v_exp_f32_e32 v67, v67
	ds_read_b128 v[172:175], v210 offset:18432
	v_mfma_f32_16x16x32_bf16 v[48:51], v[180:183], v[216:219], v[48:51]
	v_exp_f32_e32 v71, v71
	v_mfma_f32_16x16x32_bf16 v[52:55], v[180:183], v[238:241], v[52:55]
	v_add_f32_e32 v220, v64, v65
	ds_read_b128 v[176:179], v203 offset:40960
	s_waitcnt lgkmcnt(5)
	v_mfma_f32_16x16x32_bf16 v[76:79], v[230:233], v[124:127], v[76:79]
	v_add_f32_e32 v221, v68, v69
	v_mfma_f32_16x16x32_bf16 v[72:75], v[230:233], v[108:111], v[72:75]
	v_add_f32_e32 v220, v220, v66
	ds_read_b128 v[180:183], v210 offset:20480
	v_mfma_f32_16x16x32_bf16 v[60:63], v[234:237], v[238:241], v[60:63]
	v_add_f32_e32 v221, v221, v70
	v_add_f32_e32 v220, v220, v67
	v_mfma_f32_16x16x32_bf16 v[56:59], v[234:237], v[216:219], v[56:59]
	v_add_f32_e32 v221, v221, v71
	ds_read_b128 v[230:233], v246 offset:40960
	s_waitcnt lgkmcnt(5)
	v_mfma_f32_16x16x32_bf16 v[80:83], v[160:163], v[96:99], 0
	v_exp_f32_e32 v72, v72
	v_mfma_f32_16x16x32_bf16 v[84:87], v[160:163], v[112:115], 0
	v_exp_f32_e32 v76, v76
	ds_read_b128 v[234:237], v210 offset:22528
	v_mfma_f32_16x16x32_bf16 v[0:3], v[164:167], v[242:245], v[0:3]
	v_exp_f32_e32 v73, v73
	v_mfma_f32_16x16x32_bf16 v[4:7], v[164:167], v[204:207], v[4:7]
	v_exp_f32_e32 v77, v77
	ds_read_b128 v[160:163], v201 offset:45056
	s_waitcnt lgkmcnt(5)
	v_mfma_f32_16x16x32_bf16 v[84:87], v[168:171], v[116:119], v[84:87]
	v_exp_f32_e32 v74, v74
	v_mfma_f32_16x16x32_bf16 v[80:83], v[168:171], v[100:103], v[80:83]
	v_exp_f32_e32 v78, v78
	ds_read_b128 v[164:167], v210 offset:24576
	v_mfma_f32_16x16x32_bf16 v[12:15], v[172:175], v[204:207], v[12:15]
	v_exp_f32_e32 v75, v75
	v_mfma_f32_16x16x32_bf16 v[8:11], v[172:175], v[242:245], v[8:11]
	v_exp_f32_e32 v79, v79
	ds_read_b128 v[168:171], v202 offset:45056
	s_waitcnt lgkmcnt(5)
	v_mfma_f32_16x16x32_bf16 v[80:83], v[176:179], v[104:107], v[80:83]
	v_add_f32_e32 v220, v220, v72
	v_add_f32_e32 v221, v221, v76
	v_mfma_f32_16x16x32_bf16 v[84:87], v[176:179], v[120:123], v[84:87]
	v_add_f32_e32 v220, v220, v73
	ds_read_b128 v[172:175], v210 offset:26624
	v_mfma_f32_16x16x32_bf16 v[16:19], v[180:183], v[242:245], v[16:19]
	v_add_f32_e32 v221, v221, v77
	v_add_f32_e32 v220, v220, v74
	v_mfma_f32_16x16x32_bf16 v[20:23], v[180:183], v[204:207], v[20:23]
	v_add_f32_e32 v221, v221, v78
	ds_read_b128 v[176:179], v203 offset:45056
	s_waitcnt lgkmcnt(5)
	v_mfma_f32_16x16x32_bf16 v[84:87], v[230:233], v[124:127], v[84:87]
	v_add_f32_e32 v220, v220, v75
	v_add_f32_e32 v221, v221, v79
	v_mfma_f32_16x16x32_bf16 v[80:83], v[230:233], v[108:111], v[80:83]
	v_cvt_pk_bf16_f32 v216, v64, v65
	ds_read_b128 v[180:183], v210 offset:28672
	v_mfma_f32_16x16x32_bf16 v[28:31], v[234:237], v[204:207], v[28:31]
	v_cvt_pk_bf16_f32 v217, v66, v67
	v_cvt_pk_bf16_f32 v238, v68, v69
	v_mfma_f32_16x16x32_bf16 v[24:27], v[234:237], v[242:245], v[24:27]
	v_cvt_pk_bf16_f32 v239, v70, v71
	ds_read_b128 v[230:233], v246 offset:45056
	s_waitcnt lgkmcnt(5)
	v_mfma_f32_16x16x32_bf16 v[88:91], v[160:163], v[96:99], 0
	v_exp_f32_e32 v80, v80
	v_mfma_f32_16x16x32_bf16 v[92:95], v[160:163], v[112:115], 0
	v_exp_f32_e32 v84, v84
	ds_read_b128 v[234:237], v210 offset:30720
	v_mfma_f32_16x16x32_bf16 v[32:35], v[164:167], v[242:245], v[32:35]
	v_exp_f32_e32 v81, v81
	v_mfma_f32_16x16x32_bf16 v[36:39], v[164:167], v[204:207], v[36:39]
	v_exp_f32_e32 v85, v85
	s_waitcnt lgkmcnt(4)
	v_mfma_f32_16x16x32_bf16 v[92:95], v[168:171], v[116:119], v[92:95]
	v_exp_f32_e32 v82, v82
	v_mfma_f32_16x16x32_bf16 v[88:91], v[168:171], v[100:103], v[88:91]
	v_exp_f32_e32 v86, v86
	v_mfma_f32_16x16x32_bf16 v[44:47], v[172:175], v[204:207], v[44:47]
	v_exp_f32_e32 v83, v83
	v_mfma_f32_16x16x32_bf16 v[40:43], v[172:175], v[242:245], v[40:43]
	v_exp_f32_e32 v87, v87
	s_waitcnt lgkmcnt(3)
	v_mfma_f32_16x16x32_bf16 v[88:91], v[176:179], v[104:107], v[88:91]
	v_add_f32_e32 v220, v220, v80
	v_add_f32_e32 v221, v221, v84
	v_mfma_f32_16x16x32_bf16 v[92:95], v[176:179], v[120:123], v[92:95]
	v_add_f32_e32 v220, v220, v81
	s_waitcnt lgkmcnt(0)
	s_barrier
	ds_read_b128 v[160:163], v201 offset:49152
	ds_read_b128 v[164:167], v209 offset:32768
	ds_read_b128 v[168:171], v202 offset:49152
	ds_read_b128 v[172:175], v209 offset:34816
	v_mfma_f32_16x16x32_bf16 v[48:51], v[180:183], v[242:245], v[48:51]
	v_add_f32_e32 v221, v221, v85
	v_add_f32_e32 v220, v220, v82
	v_mfma_f32_16x16x32_bf16 v[52:55], v[180:183], v[204:207], v[52:55]
	v_add_f32_e32 v221, v221, v86
	ds_read_b128 v[176:179], v203 offset:49152
	v_mfma_f32_16x16x32_bf16 v[92:95], v[230:233], v[124:127], v[92:95]
	v_add_f32_e32 v220, v220, v83
	v_add_f32_e32 v221, v221, v87
	v_mfma_f32_16x16x32_bf16 v[88:91], v[230:233], v[108:111], v[88:91]
	v_cvt_pk_bf16_f32 v218, v72, v73
	ds_read_b128 v[180:183], v209 offset:36864
	v_mfma_f32_16x16x32_bf16 v[60:63], v[234:237], v[204:207], v[60:63]
	v_cvt_pk_bf16_f32 v219, v74, v75
	v_cvt_pk_bf16_f32 v240, v76, v77
	v_mfma_f32_16x16x32_bf16 v[56:59], v[234:237], v[242:245], v[56:59]
	v_cvt_pk_bf16_f32 v241, v78, v79
	ds_read_b128 v[230:233], v246 offset:49152
	s_cmp_eq_u32 s100, 0
	s_cbranch_scc1 .Lattn_pa2
	s_setprio 1
	s_branch .Lattn_pb2

.Lattn_pb2:
	s_waitcnt lgkmcnt(5)
	v_mfma_f32_16x16x32_bf16 v[64:67], v[160:163], v[96:99], 0
	v_exp_f32_e32 v88, v88
	v_mfma_f32_16x16x32_bf16 v[68:71], v[160:163], v[112:115], 0
	v_exp_f32_e32 v92, v92
	ds_read_b128 v[234:237], v209 offset:38912
	s_add_u32 s8, s16, 0x3bc00300
	s_addc_u32 s9, s17, 0
	s_add_u32 s6, s15, 0x23a70000
	s_addc_u32 s7, s14, 0
	v_mfma_f32_16x16x32_bf16 v[0:3], v[164:167], v[216:219], v[0:3]
	v_cvt_pk_bf16_f32 v242, v80, v81
	v_mfma_f32_16x16x32_bf16 v[4:7], v[164:167], v[238:241], v[4:7]
	v_exp_f32_e32 v89, v89
	ds_read_b128 v[160:163], v201 offset:53248
	s_waitcnt vmcnt(4)
	ds_write_b128 v225, v[152:155] offset:16384
	s_waitcnt lgkmcnt(6)
	v_mfma_f32_16x16x32_bf16 v[68:71], v[168:171], v[116:119], v[68:71]
	v_exp_f32_e32 v93, v93
	v_mfma_f32_16x16x32_bf16 v[64:67], v[168:171], v[100:103], v[64:67]
	v_cvt_pk_bf16_f32 v243, v82, v83
	ds_read_b128 v[164:167], v209 offset:40960
	ds_write_b128 v226, v[156:159] offset:16384
	v_mfma_f32_16x16x32_bf16 v[12:15], v[172:175], v[238:241], v[12:15]
	v_exp_f32_e32 v90, v90
	v_mfma_f32_16x16x32_bf16 v[8:11], v[172:175], v[216:219], v[8:11]
	v_exp_f32_e32 v94, v94
	ds_read_b128 v[168:171], v202 offset:53248
	ds_write_b64 v227, v[132:133] offset:0
	s_waitcnt lgkmcnt(8)
	v_mfma_f32_16x16x32_bf16 v[64:67], v[176:179], v[104:107], v[64:67]
	v_cvt_pk_bf16_f32 v204, v84, v85
	v_mfma_f32_16x16x32_bf16 v[68:71], v[176:179], v[120:123], v[68:71]
	v_exp_f32_e32 v91, v91
	ds_read_b128 v[172:175], v209 offset:43008
	ds_write_b64 v228, v[134:135] offset:0
	v_mfma_f32_16x16x32_bf16 v[16:19], v[180:183], v[216:219], v[16:19]
	v_exp_f32_e32 v95, v95
	v_mfma_f32_16x16x32_bf16 v[20:23], v[180:183], v[238:241], v[20:23]
	v_cvt_pk_bf16_f32 v205, v86, v87
	v_add_f32_e32 v220, v220, v88
	ds_read_b128 v[176:179], v203 offset:53248
	ds_write_b64 v229, v[128:129] offset:0
	s_waitcnt lgkmcnt(10)
	v_mfma_f32_16x16x32_bf16 v[68:71], v[230:233], v[124:127], v[68:71]
	v_add_f32_e32 v221, v221, v92
	v_add_f32_e32 v220, v220, v89
	v_mfma_f32_16x16x32_bf16 v[64:67], v[230:233], v[108:111], v[64:67]
	v_add_f32_e32 v221, v221, v93
	v_cvt_pk_bf16_f32 v244, v88, v89
	ds_read_b128 v[180:183], v209 offset:45056
	ds_write_b64 v184, v[130:131] offset:0
	v_mfma_f32_16x16x32_bf16 v[28:31], v[234:237], v[238:241], v[28:31]
	v_cvt_pk_bf16_f32 v245, v90, v91
	v_cvt_pk_bf16_f32 v206, v92, v93
	v_mfma_f32_16x16x32_bf16 v[24:27], v[234:237], v[216:219], v[24:27]
	v_cvt_pk_bf16_f32 v207, v94, v95
	ds_read_b128 v[230:233], v246 offset:53248
	global_load_dwordx4 v[132:135], v198, s[8:9]
	s_waitcnt lgkmcnt(10)
	v_mfma_f32_16x16x32_bf16 v[72:75], v[160:163], v[96:99], 0
	v_add_f32_e32 v220, v220, v90
	v_add_f32_e32 v221, v221, v94
	v_mfma_f32_16x16x32_bf16 v[76:79], v[160:163], v[112:115], 0
	v_add_f32_e32 v220, v220, v91
	v_add_f32_e32 v221, v221, v95
	ds_read_b128 v[234:237], v209 offset:47104
	global_load_dwordx4 v[128:131], v199, s[8:9]
	v_mfma_f32_16x16x32_bf16 v[32:35], v[164:167], v[216:219], v[32:35]
	v_add_f32_e32 v194, v194, v220
	v_add_f32_e32 v195, v195, v221
	v_mfma_f32_16x16x32_bf16 v[36:39], v[164:167], v[238:241], v[36:39]
	v_exp_f32_e32 v64, v64
	ds_read_b128 v[160:163], v201 offset:57344
	global_load_dwordx4 v[152:155], v196, s[6:7]
	s_waitcnt lgkmcnt(8)
	v_mfma_f32_16x16x32_bf16 v[76:79], v[168:171], v[116:119], v[76:79]
	v_exp_f32_e32 v68, v68
	v_mfma_f32_16x16x32_bf16 v[72:75], v[168:171], v[100:103], v[72:75]
	v_exp_f32_e32 v65, v65
	ds_read_b128 v[164:167], v210 offset:32768
	global_load_dwordx4 v[156:159], v197, s[6:7]
	v_mfma_f32_16x16x32_bf16 v[44:47], v[172:175], v[238:241], v[44:47]
	v_exp_f32_e32 v69, v69
	v_mfma_f32_16x16x32_bf16 v[40:43], v[172:175], v[216:219], v[40:43]
	v_exp_f32_e32 v66, v66
	ds_read_b128 v[168:171], v202 offset:57344
	s_waitcnt lgkmcnt(6)
	v_mfma_f32_16x16x32_bf16 v[72:75], v[176:179], v[104:107], v[72:75]
	v_exp_f32_e32 v70, v70
	v_mfma_f32_16x16x32_bf16 v[76:79], v[176:179], v[120:123], v[76:79]
	v_exp_f32_e32 v67, v67
	ds_read_b128 v[172:175], v210 offset:34816
	v_mfma_f32_16x16x32_bf16 v[48:51], v[180:183], v[216:219], v[48:51]
	v_exp_f32_e32 v71, v71
	v_mfma_f32_16x16x32_bf16 v[52:55], v[180:183], v[238:241], v[52:55]
	v_add_f32_e32 v220, v64, v65
	ds_read_b128 v[176:179], v203 offset:57344
	s_waitcnt lgkmcnt(5)
	v_mfma_f32_16x16x32_bf16 v[76:79], v[230:233], v[124:127], v[76:79]
	v_add_f32_e32 v221, v68, v69
	v_mfma_f32_16x16x32_bf16 v[72:75], v[230:233], v[108:111], v[72:75]
	v_add_f32_e32 v220, v220, v66
	ds_read_b128 v[180:183], v210 offset:36864
	v_mfma_f32_16x16x32_bf16 v[60:63], v[234:237], v[238:241], v[60:63]
	v_add_f32_e32 v221, v221, v70
	v_add_f32_e32 v220, v220, v67
	v_mfma_f32_16x16x32_bf16 v[56:59], v[234:237], v[216:219], v[56:59]
	v_add_f32_e32 v221, v221, v71
	ds_read_b128 v[230:233], v246 offset:57344
	s_waitcnt lgkmcnt(5)
	v_mfma_f32_16x16x32_bf16 v[80:83], v[160:163], v[96:99], 0
	v_exp_f32_e32 v72, v72
	v_mfma_f32_16x16x32_bf16 v[84:87], v[160:163], v[112:115], 0
	v_exp_f32_e32 v76, v76
	ds_read_b128 v[234:237], v210 offset:38912
	v_mfma_f32_16x16x32_bf16 v[0:3], v[164:167], v[242:245], v[0:3]
	v_exp_f32_e32 v73, v73
	v_mfma_f32_16x16x32_bf16 v[4:7], v[164:167], v[204:207], v[4:7]
	v_exp_f32_e32 v77, v77
	ds_read_b128 v[160:163], v201 offset:61440
	s_waitcnt lgkmcnt(5)
	v_mfma_f32_16x16x32_bf16 v[84:87], v[168:171], v[116:119], v[84:87]
	v_exp_f32_e32 v74, v74
	v_mfma_f32_16x16x32_bf16 v[80:83], v[168:171], v[100:103], v[80:83]
	v_exp_f32_e32 v78, v78
	ds_read_b128 v[164:167], v210 offset:40960
	v_mfma_f32_16x16x32_bf16 v[12:15], v[172:175], v[204:207], v[12:15]
	v_exp_f32_e32 v75, v75
	v_mfma_f32_16x16x32_bf16 v[8:11], v[172:175], v[242:245], v[8:11]
	v_exp_f32_e32 v79, v79
	ds_read_b128 v[168:171], v202 offset:61440
	s_waitcnt lgkmcnt(5)
	v_mfma_f32_16x16x32_bf16 v[80:83], v[176:179], v[104:107], v[80:83]
	v_add_f32_e32 v220, v220, v72
	v_add_f32_e32 v221, v221, v76
	v_mfma_f32_16x16x32_bf16 v[84:87], v[176:179], v[120:123], v[84:87]
	v_add_f32_e32 v220, v220, v73
	ds_read_b128 v[172:175], v210 offset:43008
	v_mfma_f32_16x16x32_bf16 v[16:19], v[180:183], v[242:245], v[16:19]
	v_add_f32_e32 v221, v221, v77
	v_add_f32_e32 v220, v220, v74
	v_mfma_f32_16x16x32_bf16 v[20:23], v[180:183], v[204:207], v[20:23]
	v_add_f32_e32 v221, v221, v78
	ds_read_b128 v[176:179], v203 offset:61440
	s_waitcnt lgkmcnt(5)
	v_mfma_f32_16x16x32_bf16 v[84:87], v[230:233], v[124:127], v[84:87]
	v_add_f32_e32 v220, v220, v75
	v_add_f32_e32 v221, v221, v79
	v_mfma_f32_16x16x32_bf16 v[80:83], v[230:233], v[108:111], v[80:83]
	v_cvt_pk_bf16_f32 v216, v64, v65
	ds_read_b128 v[180:183], v210 offset:45056
	v_mfma_f32_16x16x32_bf16 v[28:31], v[234:237], v[204:207], v[28:31]
	v_cvt_pk_bf16_f32 v217, v66, v67
	v_cvt_pk_bf16_f32 v238, v68, v69
	v_mfma_f32_16x16x32_bf16 v[24:27], v[234:237], v[242:245], v[24:27]
	v_cvt_pk_bf16_f32 v239, v70, v71
	ds_read_b128 v[230:233], v246 offset:61440
	s_waitcnt lgkmcnt(5)
	v_mfma_f32_16x16x32_bf16 v[88:91], v[160:163], v[96:99], 0
	v_exp_f32_e32 v80, v80
	v_mfma_f32_16x16x32_bf16 v[92:95], v[160:163], v[112:115], 0
	v_exp_f32_e32 v84, v84
	ds_read_b128 v[234:237], v210 offset:47104
	v_mfma_f32_16x16x32_bf16 v[32:35], v[164:167], v[242:245], v[32:35]
	v_exp_f32_e32 v81, v81
	v_mfma_f32_16x16x32_bf16 v[36:39], v[164:167], v[204:207], v[36:39]
	v_exp_f32_e32 v85, v85
	ds_read_b128 v[160:163], v201 offset:0
	s_waitcnt lgkmcnt(5)
	v_mfma_f32_16x16x32_bf16 v[92:95], v[168:171], v[116:119], v[92:95]
	v_exp_f32_e32 v82, v82
	v_mfma_f32_16x16x32_bf16 v[88:91], v[168:171], v[100:103], v[88:91]
	v_exp_f32_e32 v86, v86
	ds_read_b128 v[164:167], v209 offset:49152
	v_mfma_f32_16x16x32_bf16 v[44:47], v[172:175], v[204:207], v[44:47]
	v_exp_f32_e32 v83, v83
	v_mfma_f32_16x16x32_bf16 v[40:43], v[172:175], v[242:245], v[40:43]
	v_exp_f32_e32 v87, v87
	ds_read_b128 v[168:171], v202 offset:0
	s_waitcnt lgkmcnt(5)
	v_mfma_f32_16x16x32_bf16 v[88:91], v[176:179], v[104:107], v[88:91]
	v_add_f32_e32 v220, v220, v80
	v_add_f32_e32 v221, v221, v84
	v_mfma_f32_16x16x32_bf16 v[92:95], v[176:179], v[120:123], v[92:95]
	v_add_f32_e32 v220, v220, v81
	ds_read_b128 v[172:175], v209 offset:51200
	v_mfma_f32_16x16x32_bf16 v[48:51], v[180:183], v[242:245], v[48:51]
	v_add_f32_e32 v221, v221, v85
	v_add_f32_e32 v220, v220, v82
	v_mfma_f32_16x16x32_bf16 v[52:55], v[180:183], v[204:207], v[52:55]
	v_add_f32_e32 v221, v221, v86
	ds_read_b128 v[176:179], v203 offset:0
	s_waitcnt lgkmcnt(5)
	v_mfma_f32_16x16x32_bf16 v[92:95], v[230:233], v[124:127], v[92:95]
	v_add_f32_e32 v220, v220, v83
	v_add_f32_e32 v221, v221, v87
	v_mfma_f32_16x16x32_bf16 v[88:91], v[230:233], v[108:111], v[88:91]
	v_cvt_pk_bf16_f32 v218, v72, v73
	ds_read_b128 v[180:183], v209 offset:53248
	v_mfma_f32_16x16x32_bf16 v[60:63], v[234:237], v[204:207], v[60:63]
	v_cvt_pk_bf16_f32 v219, v74, v75
	v_cvt_pk_bf16_f32 v240, v76, v77
	v_mfma_f32_16x16x32_bf16 v[56:59], v[234:237], v[242:245], v[56:59]
	v_cvt_pk_bf16_f32 v241, v78, v79
	ds_read_b128 v[230:233], v246 offset:0
	s_cmp_eq_u32 s100, 1
	s_cbranch_scc1 .Lattn_pa3
	s_setprio 1
	s_branch .Lattn_pb3

.Lattn_pb3:
	s_waitcnt lgkmcnt(5)
	v_mfma_f32_16x16x32_bf16 v[64:67], v[160:163], v[96:99], 0
	v_exp_f32_e32 v88, v88
	v_mfma_f32_16x16x32_bf16 v[68:71], v[160:163], v[112:115], 0
	v_exp_f32_e32 v92, v92
	ds_read_b128 v[234:237], v209 offset:55296
	s_add_u32 s8, s16, 0x3bc00380
	s_addc_u32 s9, s17, 0
	s_add_u32 s6, s15, 0x23a80000
	s_addc_u32 s7, s14, 0
	v_mfma_f32_16x16x32_bf16 v[0:3], v[164:167], v[216:219], v[0:3]
	v_cvt_pk_bf16_f32 v242, v80, v81
	v_mfma_f32_16x16x32_bf16 v[4:7], v[164:167], v[238:241], v[4:7]
	v_exp_f32_e32 v89, v89
	ds_read_b128 v[160:163], v201 offset:4096
	s_waitcnt vmcnt(4)
	ds_write_b128 v225, v[136:139] offset:32768
	s_waitcnt lgkmcnt(6)
	v_mfma_f32_16x16x32_bf16 v[68:71], v[168:171], v[116:119], v[68:71]
	v_exp_f32_e32 v93, v93
	v_mfma_f32_16x16x32_bf16 v[64:67], v[168:171], v[100:103], v[64:67]
	v_cvt_pk_bf16_f32 v243, v82, v83
	ds_read_b128 v[164:167], v209 offset:57344
	ds_write_b128 v226, v[140:143] offset:32768
	v_mfma_f32_16x16x32_bf16 v[12:15], v[172:175], v[238:241], v[12:15]
	v_exp_f32_e32 v90, v90
	v_mfma_f32_16x16x32_bf16 v[8:11], v[172:175], v[216:219], v[8:11]
	v_exp_f32_e32 v94, v94
	ds_read_b128 v[168:171], v202 offset:4096
	ds_write_b64 v227, v[148:149] offset:16384
	s_waitcnt lgkmcnt(8)
	v_mfma_f32_16x16x32_bf16 v[64:67], v[176:179], v[104:107], v[64:67]
	v_cvt_pk_bf16_f32 v204, v84, v85
	v_mfma_f32_16x16x32_bf16 v[68:71], v[176:179], v[120:123], v[68:71]
	v_exp_f32_e32 v91, v91
	ds_read_b128 v[172:175], v209 offset:59392
	ds_write_b64 v228, v[150:151] offset:16384
	v_mfma_f32_16x16x32_bf16 v[16:19], v[180:183], v[216:219], v[16:19]
	v_exp_f32_e32 v95, v95
	v_mfma_f32_16x16x32_bf16 v[20:23], v[180:183], v[238:241], v[20:23]
	v_cvt_pk_bf16_f32 v205, v86, v87
	v_add_f32_e32 v220, v220, v88
	ds_read_b128 v[176:179], v203 offset:4096
	ds_write_b64 v229, v[144:145] offset:16384
	s_waitcnt lgkmcnt(10)
	v_mfma_f32_16x16x32_bf16 v[68:71], v[230:233], v[124:127], v[68:71]
	v_add_f32_e32 v221, v221, v92
	v_add_f32_e32 v220, v220, v89
	v_mfma_f32_16x16x32_bf16 v[64:67], v[230:233], v[108:111], v[64:67]
	v_add_f32_e32 v221, v221, v93
	v_cvt_pk_bf16_f32 v244, v88, v89
	ds_read_b128 v[180:183], v209 offset:61440
	ds_write_b64 v184, v[146:147] offset:16384
	v_mfma_f32_16x16x32_bf16 v[28:31], v[234:237], v[238:241], v[28:31]
	v_cvt_pk_bf16_f32 v245, v90, v91
	v_cvt_pk_bf16_f32 v206, v92, v93
	v_mfma_f32_16x16x32_bf16 v[24:27], v[234:237], v[216:219], v[24:27]
	v_cvt_pk_bf16_f32 v207, v94, v95
	ds_read_b128 v[230:233], v246 offset:4096
	global_load_dwordx4 v[148:151], v198, s[8:9]
	s_waitcnt lgkmcnt(10)
	v_mfma_f32_16x16x32_bf16 v[72:75], v[160:163], v[96:99], 0
	v_add_f32_e32 v220, v220, v90
	v_add_f32_e32 v221, v221, v94
	v_mfma_f32_16x16x32_bf16 v[76:79], v[160:163], v[112:115], 0
	v_add_f32_e32 v220, v220, v91
	v_add_f32_e32 v221, v221, v95
	ds_read_b128 v[234:237], v209 offset:63488
	global_load_dwordx4 v[144:147], v199, s[8:9]
	v_mfma_f32_16x16x32_bf16 v[32:35], v[164:167], v[216:219], v[32:35]
	v_add_f32_e32 v194, v194, v220
	v_add_f32_e32 v195, v195, v221
	v_mfma_f32_16x16x32_bf16 v[36:39], v[164:167], v[238:241], v[36:39]
	v_exp_f32_e32 v64, v64
	ds_read_b128 v[160:163], v201 offset:8192
	global_load_dwordx4 v[136:139], v196, s[6:7]
	s_waitcnt lgkmcnt(8)
	v_mfma_f32_16x16x32_bf16 v[76:79], v[168:171], v[116:119], v[76:79]
	v_exp_f32_e32 v68, v68
	v_mfma_f32_16x16x32_bf16 v[72:75], v[168:171], v[100:103], v[72:75]
	v_exp_f32_e32 v65, v65
	ds_read_b128 v[164:167], v210 offset:49152
	global_load_dwordx4 v[140:143], v197, s[6:7]
	v_mfma_f32_16x16x32_bf16 v[44:47], v[172:175], v[238:241], v[44:47]
	v_exp_f32_e32 v69, v69
	v_mfma_f32_16x16x32_bf16 v[40:43], v[172:175], v[216:219], v[40:43]
	v_exp_f32_e32 v66, v66
	ds_read_b128 v[168:171], v202 offset:8192
	s_waitcnt lgkmcnt(6)
	v_mfma_f32_16x16x32_bf16 v[72:75], v[176:179], v[104:107], v[72:75]
	v_exp_f32_e32 v70, v70
	v_mfma_f32_16x16x32_bf16 v[76:79], v[176:179], v[120:123], v[76:79]
	v_exp_f32_e32 v67, v67
	ds_read_b128 v[172:175], v210 offset:51200
	v_mfma_f32_16x16x32_bf16 v[48:51], v[180:183], v[216:219], v[48:51]
	v_exp_f32_e32 v71, v71
	v_mfma_f32_16x16x32_bf16 v[52:55], v[180:183], v[238:241], v[52:55]
	v_add_f32_e32 v220, v64, v65
	ds_read_b128 v[176:179], v203 offset:8192
	s_waitcnt lgkmcnt(5)
	v_mfma_f32_16x16x32_bf16 v[76:79], v[230:233], v[124:127], v[76:79]
	v_add_f32_e32 v221, v68, v69
	v_mfma_f32_16x16x32_bf16 v[72:75], v[230:233], v[108:111], v[72:75]
	v_add_f32_e32 v220, v220, v66
	ds_read_b128 v[180:183], v210 offset:53248
	v_mfma_f32_16x16x32_bf16 v[60:63], v[234:237], v[238:241], v[60:63]
	v_add_f32_e32 v221, v221, v70
	v_add_f32_e32 v220, v220, v67
	v_mfma_f32_16x16x32_bf16 v[56:59], v[234:237], v[216:219], v[56:59]
	v_add_f32_e32 v221, v221, v71
	ds_read_b128 v[230:233], v246 offset:8192
	s_waitcnt lgkmcnt(5)
	v_mfma_f32_16x16x32_bf16 v[80:83], v[160:163], v[96:99], 0
	v_exp_f32_e32 v72, v72
	v_mfma_f32_16x16x32_bf16 v[84:87], v[160:163], v[112:115], 0
	v_exp_f32_e32 v76, v76
	ds_read_b128 v[234:237], v210 offset:55296
	v_mfma_f32_16x16x32_bf16 v[0:3], v[164:167], v[242:245], v[0:3]
	v_exp_f32_e32 v73, v73
	v_mfma_f32_16x16x32_bf16 v[4:7], v[164:167], v[204:207], v[4:7]
	v_exp_f32_e32 v77, v77
	ds_read_b128 v[160:163], v201 offset:12288
	s_waitcnt lgkmcnt(5)
	v_mfma_f32_16x16x32_bf16 v[84:87], v[168:171], v[116:119], v[84:87]
	v_exp_f32_e32 v74, v74
	v_mfma_f32_16x16x32_bf16 v[80:83], v[168:171], v[100:103], v[80:83]
	v_exp_f32_e32 v78, v78
	ds_read_b128 v[164:167], v210 offset:57344
	v_mfma_f32_16x16x32_bf16 v[12:15], v[172:175], v[204:207], v[12:15]
	v_exp_f32_e32 v75, v75
	v_mfma_f32_16x16x32_bf16 v[8:11], v[172:175], v[242:245], v[8:11]
	v_exp_f32_e32 v79, v79
	ds_read_b128 v[168:171], v202 offset:12288
	s_waitcnt lgkmcnt(5)
	v_mfma_f32_16x16x32_bf16 v[80:83], v[176:179], v[104:107], v[80:83]
	v_add_f32_e32 v220, v220, v72
	v_add_f32_e32 v221, v221, v76
	v_mfma_f32_16x16x32_bf16 v[84:87], v[176:179], v[120:123], v[84:87]
	v_add_f32_e32 v220, v220, v73
	ds_read_b128 v[172:175], v210 offset:59392
	s_add_u32 s10, s10, 0x200
	s_addc_u32 s11, s11, 0
	s_add_u32 s12, s12, 0x40000
	s_addc_u32 s13, s13, 0
	s_add_i32 s4, s4, 4
	s_cmpk_lt_u32 s4, 0x104
	s_cselect_b64 s[6:7], -1, 0
	s_and_b64 s[6:7], s[0:1], s[6:7]
	s_and_b64 vcc, exec, s[6:7]
	v_mfma_f32_16x16x32_bf16 v[16:19], v[180:183], v[242:245], v[16:19]
	v_add_f32_e32 v221, v221, v77
	v_add_f32_e32 v220, v220, v74
	v_mfma_f32_16x16x32_bf16 v[20:23], v[180:183], v[204:207], v[20:23]
	v_add_f32_e32 v221, v221, v78
	ds_read_b128 v[176:179], v203 offset:12288
	s_waitcnt lgkmcnt(5)
	v_mfma_f32_16x16x32_bf16 v[84:87], v[230:233], v[124:127], v[84:87]
	v_add_f32_e32 v220, v220, v75
	v_add_f32_e32 v221, v221, v79
	v_mfma_f32_16x16x32_bf16 v[80:83], v[230:233], v[108:111], v[80:83]
	v_cvt_pk_bf16_f32 v216, v64, v65
	ds_read_b128 v[180:183], v210 offset:61440
	v_mfma_f32_16x16x32_bf16 v[28:31], v[234:237], v[204:207], v[28:31]
	v_cvt_pk_bf16_f32 v217, v66, v67
	v_cvt_pk_bf16_f32 v238, v68, v69
	v_mfma_f32_16x16x32_bf16 v[24:27], v[234:237], v[242:245], v[24:27]
	v_cvt_pk_bf16_f32 v239, v70, v71
	ds_read_b128 v[230:233], v246 offset:12288
	s_waitcnt lgkmcnt(5)
	v_mfma_f32_16x16x32_bf16 v[88:91], v[160:163], v[96:99], 0
	v_exp_f32_e32 v80, v80
	v_mfma_f32_16x16x32_bf16 v[92:95], v[160:163], v[112:115], 0
	v_exp_f32_e32 v84, v84
	ds_read_b128 v[234:237], v210 offset:63488
	v_mfma_f32_16x16x32_bf16 v[32:35], v[164:167], v[242:245], v[32:35]
	v_exp_f32_e32 v81, v81
	v_mfma_f32_16x16x32_bf16 v[36:39], v[164:167], v[204:207], v[36:39]
	v_exp_f32_e32 v85, v85
	s_waitcnt lgkmcnt(4)
	v_mfma_f32_16x16x32_bf16 v[92:95], v[168:171], v[116:119], v[92:95]
	v_exp_f32_e32 v82, v82
	v_mfma_f32_16x16x32_bf16 v[88:91], v[168:171], v[100:103], v[88:91]
	v_exp_f32_e32 v86, v86
	v_mfma_f32_16x16x32_bf16 v[44:47], v[172:175], v[204:207], v[44:47]
	v_exp_f32_e32 v83, v83
	v_mfma_f32_16x16x32_bf16 v[40:43], v[172:175], v[242:245], v[40:43]
	v_exp_f32_e32 v87, v87
	s_waitcnt lgkmcnt(3)
	v_mfma_f32_16x16x32_bf16 v[88:91], v[176:179], v[104:107], v[88:91]
	v_add_f32_e32 v220, v220, v80
	v_add_f32_e32 v221, v221, v84
	v_mfma_f32_16x16x32_bf16 v[92:95], v[176:179], v[120:123], v[92:95]
	v_add_f32_e32 v220, v220, v81
	s_waitcnt lgkmcnt(0)
	s_barrier
	ds_read_b128 v[160:163], v201 offset:16384
	ds_read_b128 v[164:167], v209 offset:0
	ds_read_b128 v[168:171], v202 offset:16384
	ds_read_b128 v[172:175], v209 offset:2048
	v_mfma_f32_16x16x32_bf16 v[48:51], v[180:183], v[242:245], v[48:51]
	v_add_f32_e32 v221, v221, v85
	v_add_f32_e32 v220, v220, v82
	v_mfma_f32_16x16x32_bf16 v[52:55], v[180:183], v[204:207], v[52:55]
	v_add_f32_e32 v221, v221, v86
	ds_read_b128 v[176:179], v203 offset:16384
	v_mfma_f32_16x16x32_bf16 v[92:95], v[230:233], v[124:127], v[92:95]
	v_add_f32_e32 v220, v220, v83
	v_add_f32_e32 v221, v221, v87
	v_mfma_f32_16x16x32_bf16 v[88:91], v[230:233], v[108:111], v[88:91]
	v_cvt_pk_bf16_f32 v218, v72, v73
	ds_read_b128 v[180:183], v209 offset:4096
	v_mfma_f32_16x16x32_bf16 v[60:63], v[234:237], v[204:207], v[60:63]
	v_cvt_pk_bf16_f32 v219, v74, v75
	v_cvt_pk_bf16_f32 v240, v76, v77
	v_mfma_f32_16x16x32_bf16 v[56:59], v[234:237], v[242:245], v[56:59]
	v_cvt_pk_bf16_f32 v241, v78, v79
	ds_read_b128 v[230:233], v246 offset:16384
	s_cbranch_vccnz .LBB0_734
	s_setprio 0
	s_waitcnt vmcnt(0)
	s_nop 7
	s_nop 7
	ds_swizzle_b32 v64, v194 offset:swizzle(SWAP,16)
	s_waitcnt lgkmcnt(0)
	v_add_f32_e32 v194, v194, v64
	v_mov_b32_e32 v65, v194
	s_nop 1
	v_permlane32_swap_b32_e32 v194, v65
	v_add_f32_e32 v194, v194, v65
	s_nop 0
	v_rcp_f32_e32 v66, v194
	ds_swizzle_b32 v64, v195 offset:swizzle(SWAP,16)
	s_waitcnt lgkmcnt(0)
	v_add_f32_e32 v195, v195, v64
	v_mov_b32_e32 v65, v195
	s_nop 1
	v_permlane32_swap_b32_e32 v195, v65
	v_add_f32_e32 v195, v195, v65
	s_nop 0
	v_rcp_f32_e32 v67, v195
	v_readlane_b32 s100, v250, 8
	v_mbcnt_lo_u32_b32 v68, -1, 0
	v_mbcnt_hi_u32_b32 v68, -1, v68
	v_and_b32_e32 v69, 15, v68
	v_lshrrev_b32_e32 v70, 4, v68
	s_lshr_b32 s101, s100, 1
	v_add_u32_e32 v69, s101, v69
	v_lshlrev_b32_e32 v69, 12, v69
	v_and_b32_e32 v71, 1, v70
	v_lshlrev_b32_e32 v71, 5, v71
	v_and_b32_e32 v70, 2, v70
	v_lshl_add_u32 v71, v70, 3, v71
	v_add_u32_e32 v70, v69, v71
	v_add_u32_e32 v71, 0x10000, v70
	v_mul_f32_e32 v0, v0, v66
	v_mul_f32_e32 v1, v1, v66
	v_mul_f32_e32 v2, v2, v66
	v_mul_f32_e32 v3, v3, v66
	v_mul_f32_e32 v8, v8, v66
	v_mul_f32_e32 v9, v9, v66
	v_mul_f32_e32 v10, v10, v66
	v_mul_f32_e32 v11, v11, v66
	v_cvt_pk_bf16_f32 v72, v0, v1
	v_cvt_pk_bf16_f32 v73, v2, v3
	v_cvt_pk_bf16_f32 v74, v8, v9
	v_cvt_pk_bf16_f32 v75, v10, v11
	s_nop 1
	v_permlane16_swap_b32_e32 v72, v74
	v_permlane16_swap_b32_e32 v73, v75
	s_nop 1
	global_store_dwordx4 v70, v[72:75], s[58:59] offset:0
	v_mul_f32_e32 v16, v16, v66
	v_mul_f32_e32 v17, v17, v66
	v_mul_f32_e32 v18, v18, v66
	v_mul_f32_e32 v19, v19, v66
	v_mul_f32_e32 v24, v24, v66
	v_mul_f32_e32 v25, v25, v66
	v_mul_f32_e32 v26, v26, v66
	v_mul_f32_e32 v27, v27, v66
	v_cvt_pk_bf16_f32 v76, v16, v17
	v_cvt_pk_bf16_f32 v77, v18, v19
	v_cvt_pk_bf16_f32 v78, v24, v25
	v_cvt_pk_bf16_f32 v79, v26, v27
	s_nop 1
	v_permlane16_swap_b32_e32 v76, v78
	v_permlane16_swap_b32_e32 v77, v79
	s_nop 1
	global_store_dwordx4 v70, v[76:79], s[58:59] offset:64
	v_mul_f32_e32 v32, v32, v66
	v_mul_f32_e32 v33, v33, v66
	v_mul_f32_e32 v34, v34, v66
	v_mul_f32_e32 v35, v35, v66
	v_mul_f32_e32 v40, v40, v66
	v_mul_f32_e32 v41, v41, v66
	v_mul_f32_e32 v42, v42, v66
	v_mul_f32_e32 v43, v43, v66
	v_cvt_pk_bf16_f32 v80, v32, v33
	v_cvt_pk_bf16_f32 v81, v34, v35
	v_cvt_pk_bf16_f32 v82, v40, v41
	v_cvt_pk_bf16_f32 v83, v42, v43
	s_nop 1
	v_permlane16_swap_b32_e32 v80, v82
	v_permlane16_swap_b32_e32 v81, v83
	s_nop 1
	global_store_dwordx4 v70, v[80:83], s[58:59] offset:128
	v_mul_f32_e32 v48, v48, v66
	v_mul_f32_e32 v49, v49, v66
	v_mul_f32_e32 v50, v50, v66
	v_mul_f32_e32 v51, v51, v66
	v_mul_f32_e32 v56, v56, v66
	v_mul_f32_e32 v57, v57, v66
	v_mul_f32_e32 v58, v58, v66
	v_mul_f32_e32 v59, v59, v66
	v_cvt_pk_bf16_f32 v84, v48, v49
	v_cvt_pk_bf16_f32 v85, v50, v51
	v_cvt_pk_bf16_f32 v86, v56, v57
	v_cvt_pk_bf16_f32 v87, v58, v59
	s_nop 1
	v_permlane16_swap_b32_e32 v84, v86
	v_permlane16_swap_b32_e32 v85, v87
	s_nop 1
	global_store_dwordx4 v70, v[84:87], s[58:59] offset:192
	v_mul_f32_e32 v4, v4, v67
	v_mul_f32_e32 v5, v5, v67
	v_mul_f32_e32 v6, v6, v67
	v_mul_f32_e32 v7, v7, v67
	v_mul_f32_e32 v12, v12, v67
	v_mul_f32_e32 v13, v13, v67
	v_mul_f32_e32 v14, v14, v67
	v_mul_f32_e32 v15, v15, v67
	v_cvt_pk_bf16_f32 v88, v4, v5
	v_cvt_pk_bf16_f32 v89, v6, v7
	v_cvt_pk_bf16_f32 v90, v12, v13
	v_cvt_pk_bf16_f32 v91, v14, v15
	s_nop 1
	v_permlane16_swap_b32_e32 v88, v90
	v_permlane16_swap_b32_e32 v89, v91
	s_nop 1
	global_store_dwordx4 v71, v[88:91], s[58:59] offset:0
	v_mul_f32_e32 v20, v20, v67
	v_mul_f32_e32 v21, v21, v67
	v_mul_f32_e32 v22, v22, v67
	v_mul_f32_e32 v23, v23, v67
	v_mul_f32_e32 v28, v28, v67
	v_mul_f32_e32 v29, v29, v67
	v_mul_f32_e32 v30, v30, v67
	v_mul_f32_e32 v31, v31, v67
	v_cvt_pk_bf16_f32 v92, v20, v21
	v_cvt_pk_bf16_f32 v93, v22, v23
	v_cvt_pk_bf16_f32 v94, v28, v29
	v_cvt_pk_bf16_f32 v95, v30, v31
	s_nop 1
	v_permlane16_swap_b32_e32 v92, v94
	v_permlane16_swap_b32_e32 v93, v95
	s_nop 1
	global_store_dwordx4 v71, v[92:95], s[58:59] offset:64
	v_mul_f32_e32 v36, v36, v67
	v_mul_f32_e32 v37, v37, v67
	v_mul_f32_e32 v38, v38, v67
	v_mul_f32_e32 v39, v39, v67
	v_mul_f32_e32 v44, v44, v67
	v_mul_f32_e32 v45, v45, v67
	v_mul_f32_e32 v46, v46, v67
	v_mul_f32_e32 v47, v47, v67
	v_cvt_pk_bf16_f32 v72, v36, v37
	v_cvt_pk_bf16_f32 v73, v38, v39
	v_cvt_pk_bf16_f32 v74, v44, v45
	v_cvt_pk_bf16_f32 v75, v46, v47
	s_nop 1
	v_permlane16_swap_b32_e32 v72, v74
	v_permlane16_swap_b32_e32 v73, v75
	s_nop 1
	global_store_dwordx4 v71, v[72:75], s[58:59] offset:128
	v_mul_f32_e32 v52, v52, v67
	v_mul_f32_e32 v53, v53, v67
	v_mul_f32_e32 v54, v54, v67
	v_mul_f32_e32 v55, v55, v67
	v_mul_f32_e32 v60, v60, v67
	v_mul_f32_e32 v61, v61, v67
	v_mul_f32_e32 v62, v62, v67
	v_mul_f32_e32 v63, v63, v67
	v_cvt_pk_bf16_f32 v76, v52, v53
	v_cvt_pk_bf16_f32 v77, v54, v55
	v_cvt_pk_bf16_f32 v78, v60, v61
	v_cvt_pk_bf16_f32 v79, v62, v63
	s_nop 1
	v_permlane16_swap_b32_e32 v76, v78
	v_permlane16_swap_b32_e32 v77, v79
	s_nop 1
	global_store_dwordx4 v71, v[76:79], s[58:59] offset:192
	s_barrier
